# union5 + attention unit epilogue: 16 x global_store_dwordx2 per lane widened to 8 x dwordx4 with v_permlane32_swap pairs (same bytes, same addresses)
# speedup vs baseline: 1.0017x; 1.0017x over previous
; #define GAS __attribute__((address_space(1)))
; #define WG_BAR() do { asm volatile("s_waitcnt vmcnt(0) lgkmcnt(0)" ::: "memory"); __builtin_amdgcn_s_barrier(); asm volatile("" ::: "memory"); } while (0)
; __device__ __forceinline__ unsigned pk2(float lo, float hi) { f32x2_t_ v = {lo, hi}; bf16x2_t_ b = __builtin_convertvector(v, bf16x2_t_); return __builtin_bit_cast(unsigned, b); }
; __device__ __forceinline__ float half_swap_sum(float m) { unsigned a = __builtin_bit_cast(unsigned, m), b = a; half_swap(a, b); return __builtin_bit_cast(float, a) + __builtin_bit_cast(float, b); }
; __device__ __forceinline__ void attn_unit(LAS unsigned char* lds, const bf16* proj, bf16* Y, const float* relb, const float* hgain, float lam, float oscale, int b, int h, int qb, int tid, int lane, int wid, Stopwatch& sw) {
;     ...
;     WG_BAR();
;     if (mp == 0) {
;         float ss = 0.f;
; #pragma unroll
;         for (int c = 0; c < 4; ++c)
; #pragma unroll
;             for (int r = 0; r < 16; ++r) { const float d = o[c][r] * inv - lam * xch[((wq * 64 + c * 16 + r) << 6) + lane]; o[c][r] = d; ss += d * d; }
;         ss = half_swap_sum(ss);
;         const float rs = oscale / sqrtf(ss * (1.f / 128.f) + NORM_EPS);
;         bf16* yp = Y + (rowbase + qi) * LDY + 1024 + h * 128;
; #pragma unroll
;         for (int c = 0; c < 4; ++c)
; #pragma unroll
;             for (int r4 = 0; r4 < 4; ++r4) { const int dv = 32 * c + 8 * r4 + 4 * hi; const f32x4 g = *(const GAS f32x4*)(hgain + dv);
;                 v2u w; w.x = pk2(o[c][4 * r4] * rs * g.x, o[c][4 * r4 + 1] * rs * g.y); w.y = pk2(o[c][4 * r4 + 2] * rs * g.z, o[c][4 * r4 + 3] * rs * g.w);
;                 *(GAS v2u*)(yp + dv) = w; }
.LBB0_444:
	s_waitcnt vmcnt(0) lgkmcnt(0)
	s_barrier
	s_andn2_b64 vcc, exec, s[72:73]
	s_cbranch_vccnz .LBB0_343
	global_load_dwordx4 v[136:139], v2, s[74:75]
	global_load_dwordx4 v[140:143], v2, s[74:75] offset:32
	global_load_dwordx4 v[144:147], v2, s[74:75] offset:64
	global_load_dwordx4 v[152:155], v2, s[74:75] offset:96
	global_load_dwordx4 v[156:159], v2, s[74:75] offset:128
	global_load_dwordx4 v[168:171], v2, s[74:75] offset:160
	global_load_dwordx4 v[172:175], v2, s[74:75] offset:192
	global_load_dwordx4 v[176:179], v2, s[74:75] offset:224
	global_load_dwordx4 v[180:183], v2, s[74:75] offset:256
	global_load_dwordx4 v[184:187], v2, s[74:75] offset:288
	global_load_dwordx4 v[188:191], v2, s[74:75] offset:320
	global_load_dwordx4 v[192:195], v2, s[74:75] offset:352
	global_load_dwordx4 v[204:207], v2, s[74:75] offset:384
	global_load_dwordx4 v[208:211], v2, s[74:75] offset:416
	global_load_dwordx4 v[212:215], v2, s[74:75] offset:448
	global_load_dwordx4 v[216:219], v2, s[74:75] offset:480
	v_readlane_b32 s0, v253, 9
	v_readlane_b32 s24, v253, 61
	v_readlane_b32 s25, v253, 62
	v_lshl_add_u32 v76, v166, 2, s0
	ds_read2st64_b32 v[70:71], v76 offset1:1
	ds_read2st64_b32 v[68:69], v76 offset0:2 offset1:3
	ds_read2st64_b32 v[74:75], v76 offset0:4 offset1:5
	ds_read2st64_b32 v[72:73], v76 offset0:6 offset1:7
	ds_read2st64_b32 v[78:79], v76 offset0:8 offset1:9
	ds_read2st64_b32 v[82:83], v76 offset0:10 offset1:11
	s_waitcnt lgkmcnt(7)
	ds_read2st64_b32 v[126:127], v76 offset0:12 offset1:13
	s_waitcnt lgkmcnt(7)
	ds_read2st64_b32 v[128:129], v76 offset0:14 offset1:15
	ds_read2st64_b32 v[130:131], v76 offset0:16 offset1:17
	ds_read2st64_b32 v[132:133], v76 offset0:18 offset1:19
	ds_read2st64_b32 v[122:123], v76 offset0:20 offset1:21
	ds_read2st64_b32 v[124:125], v76 offset0:22 offset1:23
	ds_read2st64_b32 v[118:119], v76 offset0:24 offset1:25
	ds_read2st64_b32 v[120:121], v76 offset0:26 offset1:27
	ds_read2st64_b32 v[114:115], v76 offset0:28 offset1:29
	ds_read2st64_b32 v[116:117], v76 offset0:30 offset1:31
	ds_read2st64_b32 v[110:111], v76 offset0:32 offset1:33
	ds_read2st64_b32 v[112:113], v76 offset0:34 offset1:35
	ds_read2st64_b32 v[106:107], v76 offset0:36 offset1:37
	ds_read2st64_b32 v[108:109], v76 offset0:38 offset1:39
	ds_read2st64_b32 v[102:103], v76 offset0:40 offset1:41
	ds_read2st64_b32 v[104:105], v76 offset0:42 offset1:43
	ds_read2st64_b32 v[98:99], v76 offset0:44 offset1:45
	ds_read2st64_b32 v[100:101], v76 offset0:46 offset1:47
	ds_read2st64_b32 v[94:95], v76 offset0:48 offset1:49
	ds_read2st64_b32 v[96:97], v76 offset0:50 offset1:51
	ds_read2st64_b32 v[90:91], v76 offset0:52 offset1:53
	ds_read2st64_b32 v[92:93], v76 offset0:54 offset1:55
	ds_read2st64_b32 v[86:87], v76 offset0:56 offset1:57
	ds_read2st64_b32 v[88:89], v76 offset0:58 offset1:59
	ds_read2st64_b32 v[84:85], v76 offset0:60 offset1:61
	ds_read2st64_b32 v[76:77], v76 offset0:62 offset1:63
	s_waitcnt lgkmcnt(14)
	v_pk_mul_f32 v[68:69], v[148:149], v[68:69]
	s_lshl_b32 s34, s18, 1
	v_pk_fma_f32 v[68:69], v[54:55], v[80:81], v[68:69] op_sel_hi:[1,0,1] neg_lo:[0,0,1] neg_hi:[0,0,1]
	v_pk_mul_f32 v[54:55], v[148:149], v[70:71]
	s_waitcnt lgkmcnt(0)
	v_pk_mul_f32 v[76:77], v[148:149], v[76:77]
	v_pk_fma_f32 v[70:71], v[52:53], v[80:81], v[54:55] op_sel_hi:[1,0,1] neg_lo:[0,0,1] neg_hi:[0,0,1]
	v_pk_fma_f32 v[18:19], v[18:19], v[80:81], v[76:77] op_sel_hi:[1,0,1] neg_lo:[0,0,1] neg_hi:[0,0,1]
	v_mov_b64_e32 v[76:77], s[24:25]
	v_mad_u64_u32 v[76:77], s[24:25], v151, s67, v[76:77]
	v_mov_b32_e32 v134, v77
	v_mad_u64_u32 v[134:135], s[24:25], v163, s67, v[134:135]
	v_mul_f32_e32 v52, v71, v71
	v_mov_b32_e32 v77, v134
	v_pk_fma_f32 v[52:53], v[70:71], v[70:71], v[52:53] op_sel_hi:[1,1,0]
	v_pk_mul_f32 v[72:73], v[148:149], v[72:73]
	v_lshl_add_u64 v[76:77], v[76:77], 0, s[34:35]
	v_pk_fma_f32 v[52:53], v[68:69], v[68:69], v[52:53]
	v_mul_f32_e32 v54, v69, v69
	v_mov_b32_e32 v151, v3
	v_pk_fma_f32 v[72:73], v[58:59], v[80:81], v[72:73] op_sel_hi:[1,0,1] neg_lo:[0,0,1] neg_hi:[0,0,1]
	v_pk_mul_f32 v[58:59], v[148:149], v[74:75]
	v_pk_add_f32 v[54:55], v[52:53], v[54:55] op_sel_hi:[1,0]
	v_lshl_add_u64 v[52:53], v[76:77], 0, v[150:151]
	v_lshl_add_u64 v[52:53], v[52:53], 0, v[150:151]
	v_pk_fma_f32 v[76:77], v[56:57], v[80:81], v[58:59] op_sel_hi:[1,0,1] neg_lo:[0,0,1] neg_hi:[0,0,1]
	s_nop 0
	v_pk_fma_f32 v[54:55], v[76:77], v[76:77], v[54:55]
	v_mul_f32_e32 v56, v77, v77
	v_pk_add_f32 v[54:55], v[54:55], v[56:57] op_sel_hi:[1,0]
	v_mul_f32_e32 v56, v73, v73
	v_pk_fma_f32 v[54:55], v[72:73], v[72:73], v[54:55]
	s_nop 0
	v_pk_add_f32 v[54:55], v[54:55], v[56:57] op_sel_hi:[1,0]
	v_pk_mul_f32 v[56:57], v[148:149], v[82:83]
	s_nop 0
	v_pk_fma_f32 v[74:75], v[62:63], v[80:81], v[56:57] op_sel_hi:[1,0,1] neg_lo:[0,0,1] neg_hi:[0,0,1]
	v_pk_mul_f32 v[56:57], v[148:149], v[78:79]
	s_nop 0
	v_pk_fma_f32 v[82:83], v[60:61], v[80:81], v[56:57] op_sel_hi:[1,0,1] neg_lo:[0,0,1] neg_hi:[0,0,1]
	s_nop 0
	v_pk_fma_f32 v[54:55], v[82:83], v[82:83], v[54:55]
	v_mul_f32_e32 v56, v83, v83
	v_pk_add_f32 v[54:55], v[54:55], v[56:57] op_sel_hi:[1,0]
	v_mul_f32_e32 v56, v75, v75
	v_pk_fma_f32 v[54:55], v[74:75], v[74:75], v[54:55]
	s_nop 0
	v_pk_add_f32 v[54:55], v[54:55], v[56:57] op_sel_hi:[1,0]
	v_pk_mul_f32 v[56:57], v[148:149], v[128:129]
	s_nop 0
	v_pk_fma_f32 v[66:67], v[66:67], v[80:81], v[56:57] op_sel_hi:[1,0,1] neg_lo:[0,0,1] neg_hi:[0,0,1]
	v_pk_mul_f32 v[56:57], v[148:149], v[126:127]
	s_nop 0
	v_pk_fma_f32 v[78:79], v[64:65], v[80:81], v[56:57] op_sel_hi:[1,0,1] neg_lo:[0,0,1] neg_hi:[0,0,1]
	s_nop 0
	v_pk_fma_f32 v[54:55], v[78:79], v[78:79], v[54:55]
	v_mul_f32_e32 v56, v79, v79
; __device__ __forceinline__ void attn_unit(LAS unsigned char* lds, const bf16* proj, bf16* Y, const float* relb, const float* hgain, float lam, float oscale, int b, int h, int qb, int tid, int lane, int wid, Stopwatch& sw) {
;     ...
;         float ss = 0.f;
; #pragma unroll
;         for (int c = 0; c < 4; ++c)
; #pragma unroll
;             for (int r = 0; r < 16; ++r) { const float d = o[c][r] * inv - lam * xch[((wq * 64 + c * 16 + r) << 6) + lane]; o[c][r] = d; ss += d * d; }
	v_pk_add_f32 v[54:55], v[54:55], v[56:57] op_sel_hi:[1,0]
	v_mul_f32_e32 v56, v67, v67
	v_pk_fma_f32 v[54:55], v[66:67], v[66:67], v[54:55]
	s_nop 0
	v_pk_add_f32 v[54:55], v[54:55], v[56:57] op_sel_hi:[1,0]
	v_pk_mul_f32 v[56:57], v[148:149], v[132:133]
	s_nop 0
	v_pk_fma_f32 v[60:61], v[38:39], v[80:81], v[56:57] op_sel_hi:[1,0,1] neg_lo:[0,0,1] neg_hi:[0,0,1]
	v_pk_mul_f32 v[38:39], v[148:149], v[130:131]
	s_nop 0
	v_pk_fma_f32 v[64:65], v[36:37], v[80:81], v[38:39] op_sel_hi:[1,0,1] neg_lo:[0,0,1] neg_hi:[0,0,1]
	s_nop 0
	v_pk_fma_f32 v[36:37], v[64:65], v[64:65], v[54:55]
	v_mul_f32_e32 v38, v65, v65
	v_pk_add_f32 v[36:37], v[36:37], v[38:39] op_sel_hi:[1,0]
	v_mul_f32_e32 v38, v61, v61
	v_pk_fma_f32 v[36:37], v[60:61], v[60:61], v[36:37]
	s_nop 0
	v_pk_add_f32 v[36:37], v[36:37], v[38:39] op_sel_hi:[1,0]
	v_pk_mul_f32 v[38:39], v[148:149], v[124:125]
	s_nop 0
	v_pk_fma_f32 v[56:57], v[42:43], v[80:81], v[38:39] op_sel_hi:[1,0,1] neg_lo:[0,0,1] neg_hi:[0,0,1]
	v_pk_mul_f32 v[38:39], v[148:149], v[122:123]
	s_nop 0
	v_pk_fma_f32 v[62:63], v[40:41], v[80:81], v[38:39] op_sel_hi:[1,0,1] neg_lo:[0,0,1] neg_hi:[0,0,1]
	s_nop 0
	v_pk_fma_f32 v[36:37], v[62:63], v[62:63], v[36:37]
	v_mul_f32_e32 v38, v63, v63
	v_pk_add_f32 v[36:37], v[36:37], v[38:39] op_sel_hi:[1,0]
	v_mul_f32_e32 v38, v57, v57
	v_pk_fma_f32 v[36:37], v[56:57], v[56:57], v[36:37]
	s_nop 0
	v_pk_add_f32 v[36:37], v[36:37], v[38:39] op_sel_hi:[1,0]
	v_pk_mul_f32 v[38:39], v[148:149], v[120:121]
	s_nop 0
	v_pk_fma_f32 v[54:55], v[46:47], v[80:81], v[38:39] op_sel_hi:[1,0,1] neg_lo:[0,0,1] neg_hi:[0,0,1]
	v_pk_mul_f32 v[38:39], v[148:149], v[118:119]
	s_nop 0
	v_pk_fma_f32 v[58:59], v[44:45], v[80:81], v[38:39] op_sel_hi:[1,0,1] neg_lo:[0,0,1] neg_hi:[0,0,1]
	s_nop 0
	v_pk_fma_f32 v[36:37], v[58:59], v[58:59], v[36:37]
	v_mul_f32_e32 v38, v59, v59
	v_pk_add_f32 v[36:37], v[36:37], v[38:39] op_sel_hi:[1,0]
	v_mul_f32_e32 v38, v55, v55
	v_pk_fma_f32 v[36:37], v[54:55], v[54:55], v[36:37]
	s_nop 0
	v_pk_add_f32 v[36:37], v[36:37], v[38:39] op_sel_hi:[1,0]
	v_pk_mul_f32 v[38:39], v[148:149], v[116:117]
	s_nop 0
	v_pk_fma_f32 v[44:45], v[50:51], v[80:81], v[38:39] op_sel_hi:[1,0,1] neg_lo:[0,0,1] neg_hi:[0,0,1]
	v_pk_mul_f32 v[38:39], v[148:149], v[114:115]
	s_nop 0
	v_pk_fma_f32 v[48:49], v[48:49], v[80:81], v[38:39] op_sel_hi:[1,0,1] neg_lo:[0,0,1] neg_hi:[0,0,1]
	s_nop 0
	v_pk_fma_f32 v[36:37], v[48:49], v[48:49], v[36:37]
	v_mul_f32_e32 v38, v49, v49
	v_pk_add_f32 v[36:37], v[36:37], v[38:39] op_sel_hi:[1,0]
	v_mul_f32_e32 v38, v45, v45
	v_pk_fma_f32 v[36:37], v[44:45], v[44:45], v[36:37]
	s_nop 0
	v_pk_add_f32 v[36:37], v[36:37], v[38:39] op_sel_hi:[1,0]
	v_pk_mul_f32 v[38:39], v[148:149], v[112:113]
	s_nop 0
	v_pk_fma_f32 v[40:41], v[22:23], v[80:81], v[38:39] op_sel_hi:[1,0,1] neg_lo:[0,0,1] neg_hi:[0,0,1]
	v_pk_mul_f32 v[22:23], v[148:149], v[110:111]
	s_nop 0
	v_pk_fma_f32 v[46:47], v[20:21], v[80:81], v[22:23] op_sel_hi:[1,0,1] neg_lo:[0,0,1] neg_hi:[0,0,1]
	s_nop 0
	v_pk_fma_f32 v[20:21], v[46:47], v[46:47], v[36:37]
	v_mul_f32_e32 v22, v47, v47
	v_pk_add_f32 v[20:21], v[20:21], v[22:23] op_sel_hi:[1,0]
	v_mul_f32_e32 v22, v41, v41
	v_pk_fma_f32 v[20:21], v[40:41], v[40:41], v[20:21]
	s_nop 0
	v_pk_add_f32 v[20:21], v[20:21], v[22:23] op_sel_hi:[1,0]
	v_pk_mul_f32 v[22:23], v[148:149], v[108:109]
	s_nop 0
	v_pk_fma_f32 v[36:37], v[26:27], v[80:81], v[22:23] op_sel_hi:[1,0,1] neg_lo:[0,0,1] neg_hi:[0,0,1]
	v_pk_mul_f32 v[22:23], v[148:149], v[106:107]
	s_nop 0
	v_pk_fma_f32 v[42:43], v[24:25], v[80:81], v[22:23] op_sel_hi:[1,0,1] neg_lo:[0,0,1] neg_hi:[0,0,1]
	s_nop 0
	v_pk_fma_f32 v[20:21], v[42:43], v[42:43], v[20:21]
	v_mul_f32_e32 v22, v43, v43
	v_pk_add_f32 v[20:21], v[20:21], v[22:23] op_sel_hi:[1,0]
	v_mul_f32_e32 v22, v37, v37
	v_pk_fma_f32 v[20:21], v[36:37], v[36:37], v[20:21]
	s_nop 0
	v_pk_add_f32 v[20:21], v[20:21], v[22:23] op_sel_hi:[1,0]
	v_pk_mul_f32 v[22:23], v[148:149], v[104:105]
	s_nop 0
	v_pk_fma_f32 v[30:31], v[30:31], v[80:81], v[22:23] op_sel_hi:[1,0,1] neg_lo:[0,0,1] neg_hi:[0,0,1]
	v_pk_mul_f32 v[22:23], v[148:149], v[102:103]
	s_nop 0
	v_pk_fma_f32 v[38:39], v[28:29], v[80:81], v[22:23] op_sel_hi:[1,0,1] neg_lo:[0,0,1] neg_hi:[0,0,1]
	s_nop 0
	v_pk_fma_f32 v[20:21], v[38:39], v[38:39], v[20:21]
	v_mul_f32_e32 v22, v39, v39
	v_pk_add_f32 v[20:21], v[20:21], v[22:23] op_sel_hi:[1,0]
	v_mul_f32_e32 v22, v31, v31
	v_pk_fma_f32 v[20:21], v[30:31], v[30:31], v[20:21]
	s_nop 0
	v_pk_add_f32 v[20:21], v[20:21], v[22:23] op_sel_hi:[1,0]
	v_pk_mul_f32 v[22:23], v[148:149], v[100:101]
	s_nop 0
	v_pk_fma_f32 v[24:25], v[34:35], v[80:81], v[22:23] op_sel_hi:[1,0,1] neg_lo:[0,0,1] neg_hi:[0,0,1]
	v_pk_mul_f32 v[22:23], v[148:149], v[98:99]
	s_nop 0
	v_pk_fma_f32 v[28:29], v[32:33], v[80:81], v[22:23] op_sel_hi:[1,0,1] neg_lo:[0,0,1] neg_hi:[0,0,1]
	s_nop 0
	v_pk_fma_f32 v[20:21], v[28:29], v[28:29], v[20:21]
	v_mul_f32_e32 v22, v29, v29
	v_pk_add_f32 v[20:21], v[20:21], v[22:23] op_sel_hi:[1,0]
	v_mul_f32_e32 v22, v25, v25
	v_pk_fma_f32 v[20:21], v[24:25], v[24:25], v[20:21]
	s_nop 0
	v_pk_add_f32 v[22:23], v[20:21], v[22:23] op_sel_hi:[1,0]
	v_pk_mul_f32 v[20:21], v[148:149], v[96:97]
	s_nop 0
	v_pk_fma_f32 v[20:21], v[6:7], v[80:81], v[20:21] op_sel_hi:[1,0,1] neg_lo:[0,0,1] neg_hi:[0,0,1]
	v_pk_mul_f32 v[6:7], v[148:149], v[94:95]
	s_nop 0
	v_pk_fma_f32 v[26:27], v[4:5], v[80:81], v[6:7] op_sel_hi:[1,0,1] neg_lo:[0,0,1] neg_hi:[0,0,1]
	s_nop 0
	v_pk_fma_f32 v[4:5], v[26:27], v[26:27], v[22:23]
	v_mul_f32_e32 v6, v27, v27
	v_pk_add_f32 v[4:5], v[4:5], v[6:7] op_sel_hi:[1,0]
	v_mul_f32_e32 v6, v21, v21
	v_pk_fma_f32 v[4:5], v[20:21], v[20:21], v[4:5]
; #define GAS __attribute__((address_space(1)))
; __device__ __forceinline__ unsigned pk2(float lo, float hi) { f32x2_t_ v = {lo, hi}; bf16x2_t_ b = __builtin_convertvector(v, bf16x2_t_); return __builtin_bit_cast(unsigned, b); }
; __device__ __forceinline__ float half_swap_sum(float m) { unsigned a = __builtin_bit_cast(unsigned, m), b = a; half_swap(a, b); return __builtin_bit_cast(float, a) + __builtin_bit_cast(float, b); }
; __device__ __forceinline__ void attn_unit(LAS unsigned char* lds, const bf16* proj, bf16* Y, const float* relb, const float* hgain, float lam, float oscale, int b, int h, int qb, int tid, int lane, int wid, Stopwatch& sw) {
;     ...
;             for (int r = 0; r < 16; ++r) { const float d = o[c][r] * inv - lam * xch[((wq * 64 + c * 16 + r) << 6) + lane]; o[c][r] = d; ss += d * d; }
;         ss = half_swap_sum(ss);
;         const float rs = oscale / sqrtf(ss * (1.f / 128.f) + NORM_EPS);
;         bf16* yp = Y + (rowbase + qi) * LDY + 1024 + h * 128;
; #pragma unroll
;         for (int c = 0; c < 4; ++c)
; #pragma unroll
;             for (int r4 = 0; r4 < 4; ++r4) { const int dv = 32 * c + 8 * r4 + 4 * hi; const f32x4 g = *(const GAS f32x4*)(hgain + dv);
;                 v2u w; w.x = pk2(o[c][4 * r4] * rs * g.x, o[c][4 * r4 + 1] * rs * g.y); w.y = pk2(o[c][4 * r4 + 2] * rs * g.z, o[c][4 * r4 + 3] * rs * g.w);
	s_nop 0
	v_pk_add_f32 v[4:5], v[4:5], v[6:7] op_sel_hi:[1,0]
	v_pk_mul_f32 v[6:7], v[148:149], v[92:93]
	s_nop 0
	v_pk_fma_f32 v[10:11], v[10:11], v[80:81], v[6:7] op_sel_hi:[1,0,1] neg_lo:[0,0,1] neg_hi:[0,0,1]
	v_pk_mul_f32 v[6:7], v[148:149], v[90:91]
	s_nop 0
	v_pk_fma_f32 v[22:23], v[8:9], v[80:81], v[6:7] op_sel_hi:[1,0,1] neg_lo:[0,0,1] neg_hi:[0,0,1]
	v_pk_mul_f32 v[8:9], v[148:149], v[86:87]
	v_pk_fma_f32 v[4:5], v[22:23], v[22:23], v[4:5]
	v_mul_f32_e32 v6, v23, v23
	v_pk_add_f32 v[4:5], v[4:5], v[6:7] op_sel_hi:[1,0]
	v_mul_f32_e32 v6, v11, v11
	v_pk_fma_f32 v[4:5], v[10:11], v[10:11], v[4:5]
	v_pk_fma_f32 v[8:9], v[12:13], v[80:81], v[8:9] op_sel_hi:[1,0,1] neg_lo:[0,0,1] neg_hi:[0,0,1]
	v_pk_add_f32 v[6:7], v[4:5], v[6:7] op_sel_hi:[1,0]
	v_pk_mul_f32 v[4:5], v[148:149], v[88:89]
	v_pk_fma_f32 v[6:7], v[8:9], v[8:9], v[6:7]
	v_mul_f32_e32 v12, v9, v9
	v_pk_fma_f32 v[4:5], v[14:15], v[80:81], v[4:5] op_sel_hi:[1,0,1] neg_lo:[0,0,1] neg_hi:[0,0,1]
	v_pk_add_f32 v[6:7], v[6:7], v[12:13] op_sel_hi:[1,0]
	v_mul_f32_e32 v12, v5, v5
	v_pk_fma_f32 v[6:7], v[4:5], v[4:5], v[6:7]
	s_nop 0
	v_pk_add_f32 v[12:13], v[6:7], v[12:13] op_sel_hi:[1,0]
	v_pk_mul_f32 v[6:7], v[148:149], v[84:85]
	s_nop 0
	v_pk_fma_f32 v[6:7], v[16:17], v[80:81], v[6:7] op_sel_hi:[1,0,1] neg_lo:[0,0,1] neg_hi:[0,0,1]
	s_nop 0
	v_pk_fma_f32 v[12:13], v[6:7], v[6:7], v[12:13]
	v_mul_f32_e32 v14, v7, v7
	v_pk_add_f32 v[12:13], v[12:13], v[14:15] op_sel_hi:[1,0]
	v_mul_f32_e32 v14, v19, v19
	v_pk_fma_f32 v[12:13], v[18:19], v[18:19], v[12:13]
	s_nop 0
	v_pk_add_f32 v[12:13], v[12:13], v[14:15] op_sel_hi:[1,0]
	s_nop 0
	v_mov_b32_e32 v13, v12
	s_nop 1
	v_permlane32_swap_b32 v12, v13
	s_nop 1
	s_nop 0
	v_add_f32_e32 v12, v12, v13
	v_fmamk_f32 v12, v12, 0x3c000000, v240
	v_cmp_gt_f32_e32 vcc, s82, v12
	v_mul_f32_e32 v13, 0x4f800000, v12
	s_nop 0
	v_cndmask_b32_e32 v12, v12, v13, vcc
	v_sqrt_f32_e32 v13, v12
	s_nop 0
	v_add_u32_e32 v14, -1, v13
	v_fma_f32 v15, -v14, v13, v12
	v_cmp_ge_f32_e64 s[36:37], 0, v15
	v_add_u32_e32 v15, 1, v13
	s_nop 0
	v_cndmask_b32_e64 v14, v13, v14, s[36:37]
	v_fma_f32 v13, -v15, v13, v12
	v_cmp_lt_f32_e64 s[36:37], 0, v13
	s_nop 1
	v_cndmask_b32_e64 v13, v14, v15, s[36:37]
	v_mul_f32_e32 v14, 0x37800000, v13
	v_cndmask_b32_e32 v13, v13, v14, vcc
	v_cmp_class_f32_e32 vcc, v12, v241
	s_nop 1
	v_cndmask_b32_e32 v12, v13, v12, vcc
	v_div_scale_f32 v13, s[18:19], v12, v12, v162
	v_rcp_f32_e32 v14, v13
	s_nop 0
	v_fma_f32 v15, -v13, v14, 1.0
	v_fmac_f32_e32 v14, v15, v14
	v_div_scale_f32 v15, vcc, v162, v12, v162
	v_mul_f32_e32 v16, v15, v14
	v_fma_f32 v17, -v13, v16, v15
	v_fmac_f32_e32 v16, v17, v14
	v_fma_f32 v13, -v13, v16, v15
	v_div_fmas_f32 v13, v13, v14, v16
	v_div_fixup_f32 v12, v13, v12, v162
	v_pk_mul_f32 v[32:33], v[70:71], v[12:13] op_sel_hi:[1,0]
	v_pk_mul_f32 v[30:31], v[30:31], v[12:13] op_sel_hi:[1,0]
	v_pk_mul_f32 v[28:29], v[28:29], v[12:13] op_sel_hi:[1,0]
	v_pk_mul_f32 v[24:25], v[24:25], v[12:13] op_sel_hi:[1,0]
	v_pk_mul_f32 v[20:21], v[20:21], v[12:13] op_sel_hi:[1,0]
	v_pk_mul_f32 v[10:11], v[10:11], v[12:13] op_sel_hi:[1,0]
	v_pk_mul_f32 v[8:9], v[8:9], v[12:13] op_sel_hi:[1,0]
	v_pk_mul_f32 v[4:5], v[4:5], v[12:13] op_sel_hi:[1,0]
	s_waitcnt vmcnt(0)
; #define GAS __attribute__((address_space(1)))
; __device__ __forceinline__ unsigned pk2(float lo, float hi) { f32x2_t_ v = {lo, hi}; bf16x2_t_ b = __builtin_convertvector(v, bf16x2_t_); return __builtin_bit_cast(unsigned, b); }
; __device__ __forceinline__ void attn_unit(LAS unsigned char* lds, const bf16* proj, bf16* Y, const float* relb, const float* hgain, float lam, float oscale, int b, int h, int qb, int tid, int lane, int wid, Stopwatch& sw) {
;     ...
; #pragma unroll
;         for (int c = 0; c < 4; ++c)
; #pragma unroll
;             for (int r4 = 0; r4 < 4; ++r4) { const int dv = 32 * c + 8 * r4 + 4 * hi; const f32x4 g = *(const GAS f32x4*)(hgain + dv);
;                 v2u w; w.x = pk2(o[c][4 * r4] * rs * g.x, o[c][4 * r4 + 1] * rs * g.y); w.y = pk2(o[c][4 * r4 + 2] * rs * g.z, o[c][4 * r4 + 3] * rs * g.w);
;                 *(GAS v2u*)(yp + dv) = w; }
	v_pk_mul_f32 v[14:15], v[136:137], v[32:33]
	v_pk_mul_f32 v[32:33], v[68:69], v[12:13] op_sel_hi:[1,0]
	v_cvt_pk_bf16_f32 v220, v14, v15
	v_pk_mul_f32 v[16:17], v[138:139], v[32:33]
	v_pk_mul_f32 v[32:33], v[76:77], v[12:13] op_sel_hi:[1,0]
	v_cvt_pk_bf16_f32 v221, v16, v17
	v_pk_mul_f32 v[14:15], v[140:141], v[32:33]
	v_pk_mul_f32 v[32:33], v[72:73], v[12:13] op_sel_hi:[1,0]
	v_cvt_pk_bf16_f32 v222, v14, v15
	v_pk_mul_f32 v[16:17], v[142:143], v[32:33]
	v_pk_mul_f32 v[32:33], v[82:83], v[12:13] op_sel_hi:[1,0]
	v_cvt_pk_bf16_f32 v223, v16, v17
	s_nop 1
	v_permlane32_swap_b32 v220, v222
	v_permlane32_swap_b32 v221, v223
	global_store_dwordx4 v[52:53], v[220:223], off offset:2048
	v_pk_mul_f32 v[14:15], v[144:145], v[32:33]
	v_pk_mul_f32 v[32:33], v[74:75], v[12:13] op_sel_hi:[1,0]
	v_cvt_pk_bf16_f32 v224, v14, v15
	v_pk_mul_f32 v[16:17], v[146:147], v[32:33]
	v_pk_mul_f32 v[32:33], v[78:79], v[12:13] op_sel_hi:[1,0]
	v_cvt_pk_bf16_f32 v225, v16, v17
	v_pk_mul_f32 v[14:15], v[152:153], v[32:33]
	v_pk_mul_f32 v[32:33], v[66:67], v[12:13] op_sel_hi:[1,0]
	v_cvt_pk_bf16_f32 v226, v14, v15
	v_pk_mul_f32 v[16:17], v[154:155], v[32:33]
	v_pk_mul_f32 v[32:33], v[64:65], v[12:13] op_sel_hi:[1,0]
	v_cvt_pk_bf16_f32 v227, v16, v17
	s_nop 1
	v_permlane32_swap_b32 v224, v226
	v_permlane32_swap_b32 v225, v227
	global_store_dwordx4 v[52:53], v[224:227], off offset:2080
	v_pk_mul_f32 v[14:15], v[32:33], v[156:157]
	v_pk_mul_f32 v[32:33], v[60:61], v[12:13] op_sel_hi:[1,0]
	v_cvt_pk_bf16_f32 v220, v14, v15
	v_pk_mul_f32 v[16:17], v[32:33], v[158:159]
	v_pk_mul_f32 v[32:33], v[62:63], v[12:13] op_sel_hi:[1,0]
	v_cvt_pk_bf16_f32 v221, v16, v17
	v_pk_mul_f32 v[14:15], v[32:33], v[168:169]
	v_pk_mul_f32 v[32:33], v[56:57], v[12:13] op_sel_hi:[1,0]
	v_cvt_pk_bf16_f32 v222, v14, v15
	v_pk_mul_f32 v[16:17], v[32:33], v[170:171]
	v_pk_mul_f32 v[32:33], v[58:59], v[12:13] op_sel_hi:[1,0]
	v_cvt_pk_bf16_f32 v223, v16, v17
	s_nop 1
	v_permlane32_swap_b32 v220, v222
	v_permlane32_swap_b32 v221, v223
	global_store_dwordx4 v[52:53], v[220:223], off offset:2112
	v_pk_mul_f32 v[14:15], v[32:33], v[172:173]
	v_pk_mul_f32 v[32:33], v[54:55], v[12:13] op_sel_hi:[1,0]
	v_cvt_pk_bf16_f32 v224, v14, v15
	v_pk_mul_f32 v[16:17], v[32:33], v[174:175]
	v_pk_mul_f32 v[32:33], v[48:49], v[12:13] op_sel_hi:[1,0]
	v_cvt_pk_bf16_f32 v225, v16, v17
	v_pk_mul_f32 v[14:15], v[32:33], v[176:177]
	v_pk_mul_f32 v[32:33], v[44:45], v[12:13] op_sel_hi:[1,0]
	v_cvt_pk_bf16_f32 v226, v14, v15
	v_pk_mul_f32 v[16:17], v[32:33], v[178:179]
	v_pk_mul_f32 v[32:33], v[46:47], v[12:13] op_sel_hi:[1,0]
	v_cvt_pk_bf16_f32 v227, v16, v17
	s_nop 1
	v_permlane32_swap_b32 v224, v226
	v_permlane32_swap_b32 v225, v227
	global_store_dwordx4 v[52:53], v[224:227], off offset:2144
	v_pk_mul_f32 v[14:15], v[32:33], v[180:181]
	v_pk_mul_f32 v[32:33], v[40:41], v[12:13] op_sel_hi:[1,0]
	v_cvt_pk_bf16_f32 v220, v14, v15
	v_pk_mul_f32 v[16:17], v[32:33], v[182:183]
	v_pk_mul_f32 v[32:33], v[42:43], v[12:13] op_sel_hi:[1,0]
	v_cvt_pk_bf16_f32 v221, v16, v17
	v_pk_mul_f32 v[14:15], v[32:33], v[184:185]
	v_pk_mul_f32 v[32:33], v[36:37], v[12:13] op_sel_hi:[1,0]
	v_cvt_pk_bf16_f32 v222, v14, v15
	v_pk_mul_f32 v[16:17], v[32:33], v[186:187]
	v_pk_mul_f32 v[32:33], v[38:39], v[12:13] op_sel_hi:[1,0]
	v_cvt_pk_bf16_f32 v223, v16, v17
	s_nop 1
	v_permlane32_swap_b32 v220, v222
	v_permlane32_swap_b32 v221, v223
	global_store_dwordx4 v[52:53], v[220:223], off offset:2176
	v_pk_mul_f32 v[14:15], v[32:33], v[188:189]
	v_pk_mul_f32 v[16:17], v[30:31], v[190:191]
	v_cvt_pk_bf16_f32 v224, v14, v15
	v_cvt_pk_bf16_f32 v225, v16, v17
	v_pk_mul_f32 v[14:15], v[28:29], v[192:193]
	v_pk_mul_f32 v[16:17], v[24:25], v[194:195]
	v_cvt_pk_bf16_f32 v226, v14, v15
	v_cvt_pk_bf16_f32 v227, v16, v17
	s_nop 1
	v_permlane32_swap_b32 v224, v226
	v_permlane32_swap_b32 v225, v227
	global_store_dwordx4 v[52:53], v[224:227], off offset:2208
	v_pk_mul_f32 v[24:25], v[26:27], v[12:13] op_sel_hi:[1,0]
	v_pk_mul_f32 v[16:17], v[20:21], v[206:207]
	v_pk_mul_f32 v[14:15], v[24:25], v[204:205]
	v_pk_mul_f32 v[20:21], v[22:23], v[12:13] op_sel_hi:[1,0]
	v_cvt_pk_bf16_f32 v220, v14, v15
	v_cvt_pk_bf16_f32 v221, v16, v17
	v_pk_mul_f32 v[14:15], v[20:21], v[208:209]
	v_pk_mul_f32 v[10:11], v[10:11], v[210:211]
	v_cvt_pk_bf16_f32 v222, v14, v15
	v_cvt_pk_bf16_f32 v223, v10, v11
	s_nop 1
	v_permlane32_swap_b32 v220, v222
	v_permlane32_swap_b32 v221, v223
	global_store_dwordx4 v[52:53], v[220:223], off offset:2240
	v_pk_mul_f32 v[8:9], v[8:9], v[212:213]
	v_pk_mul_f32 v[4:5], v[4:5], v[214:215]
	v_cvt_pk_bf16_f32 v224, v8, v9
	v_cvt_pk_bf16_f32 v225, v4, v5
	v_pk_mul_f32 v[4:5], v[6:7], v[12:13] op_sel_hi:[1,0]
	v_pk_mul_f32 v[6:7], v[18:19], v[12:13] op_sel_hi:[1,0]
	v_pk_mul_f32 v[4:5], v[4:5], v[216:217]
	v_pk_mul_f32 v[6:7], v[6:7], v[218:219]
	v_cvt_pk_bf16_f32 v226, v4, v5
	v_cvt_pk_bf16_f32 v227, v6, v7
	s_nop 1
	v_permlane32_swap_b32 v224, v226
	v_permlane32_swap_b32 v225, v227
	global_store_dwordx4 v[52:53], v[224:227], off offset:2272
	s_branch .LBB0_343
